# P3 lora GEMM: skip the K tiles that only multiply zero LORAT blocks (pn<8: one 2-tile iteration at k=0; pn>=8: two iterations from k=128)
# speedup vs baseline: 1.0134x; 1.0134x over previous
;     __device__ __forceinline__ size_t aoff(const Unit& u) const { return (size_t)u.pm * a_tstep + (size_t)u.pn * a_pnstep; }
;     __device__ __forceinline__ size_t boff(const Unit& u) const { return (size_t)u.pn * b_tstep; }
;     __device__ __forceinline__ size_t boff(const Unit& u) const { return (size_t)u.pn * b_tstep; }
; #define PG8_GLOAD(dst0, dst1, lu) do { if constexpr (GATHER) { _Pragma("unroll") for (int _i = 0; _i < 2; ++_i) { dst0[_i] = S.toks[(lu) * 256 + rowA[_i]] + colA[_i]; dst1[_i] = S.toks[(lu) * 256 + 128 + rowA[_i]] + colA[_i]; } } } while (0)
; #define PG8_STAGE(bufoff, gbase, voff) do { _Pragma("unroll") for (int _i = 0; _i < 2; ++_i) \
;         __builtin_amdgcn_global_load_lds((const unsigned*)((const char*)(gbase) + (voff)[_i]), (LAS unsigned*)(lds + (bufoff) + ldsw + _i * 8192), 16, 0, 0); } while (0)
; #define PG8_BAR __builtin_amdgcn_s_barrier()
; template <class Epi, class Sched, bool ALIGN_EPI, bool SP2, bool FP8 = false>
; __device__ __forceinline__ void gemm_phase(LAS unsigned char* lds, const Gemm g, const Sched& S, const Epi& E) {
;     ...
;     for (int i = 0; i < 2; ++i) { int R, C; stage_rc(tid * 16 + i * 8192, R, C); const int Rb = Epi::PERM == 2 ? perm128(R) : (Epi::PERM ? ((R & ~31) + perm32(R & 31)) : R);
;         voffA[i] = (unsigned)(R * g.lda + C) * 2u; voffB[i] = (unsigned)(Rb * K + C) * 2u; rowA[i] = R; colA[i] = (unsigned)C * 2u; }
;     unsigned cG0[2] = {0u, 0u}, cG1[2] = {0u, 0u}, nG0[2] = {0u, 0u}, nG1[2] = {0u, 0u};
;     ...
;     const size_t kstep = (size_t)(BK * 2);
;     const size_t hstepA = (size_t)HALF * g.lda * 2, hstepB = (size_t)(Epi::PERM == 2 ? 8 : HALF) * K * 2;
;     const unsigned ldsw = (unsigned)wid * 1024u;
;     const int aoff = lds_byte(wr * 64 + fr, fq * 8), boff = lds_byte(wc * 32 + fr, fq * 8);
;     ...
;     const char* cA = (const char*)g.A + S.aoff(cur); const char* cB = (const char*)g.Bt + S.boff(cur);
;     if constexpr (SP2) {
;         PG8_GLOAD(cG0, cG1, 0);
;         PG8_STAGE(PG8_SB(0, 0), cB, voffB); PG8_STAGE(PG8_SB(0, 1), cB + hstepB, voffB); PG8_STAGE_A(PG8_SA(0, 0), cA, 0, false); PG8_STAGE_A(PG8_SA(0, 1), cA, 1, false);
;         if (wr == 1) PG8_BAR;
;         PG8_WAIT_V(2); PG8_BAR;
;         PG8_STAGE(PG8_SB(1, 0), cB + kstep, voffB); PG8_STAGE_A(PG8_SA(1, 0), cA + kstep, 0, false); PG8_STAGE(PG8_SB(1, 1), cB + hstepB + kstep, voffB);
;         PG8_WAIT_V(6); PG8_BAR;
.LBB0_369:
	s_cmp_lt_i32 s88, 4
	s_cselect_b64 s[0:1], -1, 0
	s_add_u32 s66, s26, 0x15c08000
	s_addc_u32 s67, s27, 0
	s_add_u32 s62, s26, 0x39c08000
	s_addc_u32 s63, s27, 0
	s_and_b64 s[0:1], s[0:1], s[2:3]
	s_andn2_b64 vcc, exec, s[0:1]
	s_cbranch_vccnz .LBB0_418
	v_mov_b32_e32 v18, v0
	s_cmpk_gt_i32 s18, 0x2ff
	v_readfirstlane_b32 s2, v18
	s_cbranch_scc1 .LBB0_390
	v_lshlrev_b32_e32 v1, 4, v18
	v_add_u32_e32 v2, 0x2000, v1
	v_ashrrev_i32_e32 v3, 31, v2
	v_lshrrev_b32_e32 v3, 22, v3
	v_add_u32_e32 v3, v2, v3
	v_ashrrev_i32_e32 v10, 10, v3
	v_mul_i32_i24_e32 v3, 0x400, v10
	v_sub_u32_e32 v2, v2, v3
	v_lshrrev_b32_e32 v3, 4, v2
	v_bitop3_b32 v2, v3, v2, 32 bitop3:0x6c
	v_ashrrev_i32_e32 v3, 31, v2
	v_lshrrev_b32_e32 v3, 26, v3
	v_add_u32_e32 v3, v2, v3
	v_lshlrev_b32_e32 v4, 3, v10
	v_ashrrev_i32_e32 v11, 6, v3
	v_and_b32_e32 v4, -16, v4
	v_add_u32_e32 v4, v11, v4
	v_lshlrev_b32_e32 v5, 2, v4
	v_and_b32_e32 v6, 3, v11
	v_and_or_b32 v5, v5, 48, v6
	v_lshlrev_b32_e32 v6, 1, v4
	v_lshrrev_b32_e32 v7, 2, v4
	v_and_b32_e32 v3, 0xc0, v3
	v_and_b32_e32 v6, 0x1ffffc0, v6
	v_and_b32_e32 v7, 4, v7
	v_sub_u32_e32 v2, v2, v3
	v_mov_b32_e32 v3, 1
	v_or3_b32 v5, v5, v6, v7
	v_lshlrev_b32_e32 v6, 5, v10
	v_ashrrev_i16_sdwa v2, v3, sext(v2) dst_sel:DWORD dst_unused:UNUSED_PAD src0_sel:DWORD src1_sel:BYTE_0
	s_movk_i32 s3, 0x180
	v_and_b32_e32 v12, 32, v6
	v_bfe_i32 v13, v2, 0, 16
	s_ashr_i32 s5, s2, 6
	v_mul_lo_u32 v5, v5, s3
	v_add_u32_e32 v2, v12, v13
	v_mul_lo_u32 v4, v4, s3
	s_ashr_i32 s4, s2, 8
	s_lshl_b32 s38, s5, 10
	v_add_lshl_u32 v130, v5, v2, 1
	v_add_lshl_u32 v132, v2, v4, 1
	v_bfe_i32 v2, v18, 27, 1
	s_add_u32 s39, s26, 0x5d48000
	v_lshrrev_b32_e32 v2, 22, v2
	s_addc_u32 s40, s27, 0
	v_add_u32_e32 v2, v1, v2
	v_readlane_b32 s7, v252, 38
	v_and_b32_e32 v2, 0xfffffc00, v2
	s_cmp_lt_i32 s7, 0
	s_movk_i32 s41, 0x61
	v_sub_u32_e32 v1, v1, v2
	s_cselect_b32 s6, s41, 0x60
	v_lshrrev_b32_e32 v2, 4, v1
	v_ashrrev_i32_e32 v4, 31, v18
	s_mul_i32 s6, s7, s6
	v_readlane_b32 s7, v252, 39
	v_bitop3_b32 v1, v2, v1, 32 bitop3:0x6c
	v_lshrrev_b32_e32 v4, 26, v4
	s_add_i32 s6, s6, s7
	v_ashrrev_i32_e32 v2, 31, v1
	v_add_u32_e32 v4, v18, v4
	s_mul_hi_i32 s7, s6, 0x2aaaaaab
	v_lshrrev_b32_e32 v2, 26, v2
	v_ashrrev_i32_e32 v15, 6, v4
	s_lshr_b32 s8, s7, 31
	s_ashr_i32 s7, s7, 4
	v_add_u32_e32 v2, v1, v2
	v_lshlrev_b32_e32 v4, 3, v15
	s_add_i32 s7, s7, s8
	v_ashrrev_i32_e32 v14, 6, v2
	v_and_b32_e32 v4, -16, v4
	s_lshl_b32 s8, s7, 3
	v_add_u32_e32 v4, v14, v4
	s_sub_i32 s9, 64, s8
	v_lshlrev_b32_e32 v5, 2, v4
	v_and_b32_e32 v6, 3, v14
	s_min_i32 s9, s9, 8
	v_and_or_b32 v5, v5, 48, v6
	v_lshlrev_b32_e32 v6, 1, v4
	v_lshrrev_b32_e32 v7, 2, v4
	v_and_b32_e32 v2, 0xc0, v2
	s_abs_i32 s14, s9
	v_and_b32_e32 v6, 0x1ffffc0, v6
	v_and_b32_e32 v7, 4, v7
	v_sub_u32_e32 v1, v1, v2
	v_cvt_f32_u32_e32 v2, s14
	v_or3_b32 v5, v5, v6, v7
	v_lshlrev_b32_e32 v6, 5, v15
	v_ashrrev_i16_sdwa v1, v3, sext(v1) dst_sel:DWORD dst_unused:UNUSED_PAD src0_sel:DWORD src1_sel:BYTE_0
	v_and_b32_e32 v16, 32, v6
	v_bfe_i32 v17, v1, 0, 16
	v_mul_lo_u32 v5, v5, s3
	v_add_u32_e32 v1, v16, v17
	v_mul_lo_u32 v3, v4, s3
	v_add_lshl_u32 v134, v5, v1, 1
	v_add_lshl_u32 v136, v1, v3, 1
	v_rcp_iflag_f32_e32 v1, v2
	s_sub_i32 s16, 0, s14
	s_mulk_i32 s7, 0x60
	s_sub_i32 s6, s6, s7
	v_mul_f32_e32 v1, 0x4f7ffffe, v1
	v_cvt_u32_f32_e32 v1, v1
	s_abs_i32 s15, s6
	s_xor_b32 s7, s6, s9
	s_ashr_i32 s7, s7, 31
	v_readfirstlane_b32 s17, v1
	s_mul_i32 s16, s16, s17
	s_mul_hi_u32 s16, s17, s16
	s_add_i32 s17, s17, s16
	s_mul_hi_u32 s16, s15, s17
	s_mul_i32 s17, s16, s14
	s_sub_i32 s15, s15, s17
	s_add_i32 s17, s16, 1
	s_sub_i32 s34, s15, s14
	s_cmp_ge_u32 s15, s14
	s_cselect_b32 s16, s17, s16
	s_cselect_b32 s15, s34, s15
	s_add_i32 s17, s16, 1
	s_cmp_ge_u32 s15, s14
	s_cselect_b32 s14, s17, s16
	s_xor_b32 s14, s14, s7
	s_sub_i32 s78, s14, s7
	s_mul_i32 s7, s78, s9
	s_sub_i32 s6, s6, s7
	s_add_i32 s82, s8, s6
	s_mul_i32 s7, s78, 0x30000
	s_mul_hi_i32 s6, s78, 0x30000
	s_add_u32 s80, s39, s7
	s_addc_u32 s81, s40, s6
	s_cmp_gt_i32 s78, 7
	s_cselect_b32 s99, 0x100, 0
	s_cselect_b32 s98, 0, 2
	s_add_u32 s80, s80, s99
	s_addc_u32 s81, s81, 0
	s_add_i32 s42, s38, 0
	v_mov_b32_e32 v1, 0x7f7f7f7f
	s_add_i32 m0, s42, 0x10000
	s_mul_i32 s9, s82, 0x30000
	global_load_lds_dwordx4 v134, s[80:81]
	s_add_i32 m0, s42, 0x12000
	s_add_u32 s6, s80, 0x1800
	global_load_lds_dwordx4 v130, s[80:81]
	s_addc_u32 s7, s81, 0
	s_add_i32 m0, s42, 0x14000
	s_mul_hi_i32 s8, s82, 0x30000
	global_load_lds_dwordx4 v134, s[6:7]
	s_add_i32 m0, s42, 0x16000
	s_add_u32 s76, s73, s9
	s_addc_u32 s77, s79, s8
	s_add_u32 s76, s76, s99
	s_addc_u32 s77, s77, 0
	s_add_i32 s43, s42, 0x2000
	global_load_lds_dwordx4 v130, s[6:7]
	s_mov_b32 m0, s42
	s_add_u32 s6, s76, 0x18000
	global_load_lds_dwordx4 v136, s[76:77]
	s_mov_b32 m0, s43
	s_addc_u32 s7, s77, 0
	s_add_i32 s44, s42, 0x4000
	global_load_lds_dwordx4 v132, s[76:77]
	s_mov_b32 m0, s44
	s_add_i32 s45, s42, 0x6000
	global_load_lds_dwordx4 v136, s[6:7]
	s_mov_b32 m0, s45
	v_mov_b32_e32 v135, 0
	global_load_lds_dwordx4 v132, s[6:7]
	v_mov_b32_e32 v131, v135
	v_mov_b32_e32 v137, v135
	v_mov_b32_e32 v133, v135
	s_cmp_eq_u32 s4, 1
	s_mov_b32 s46, 0
	v_lshl_add_u64 v[8:9], s[80:81], 0, v[134:135]
	v_lshl_add_u64 v[6:7], s[80:81], 0, v[130:131]
	v_lshl_add_u64 v[2:3], s[76:77], 0, v[136:137]
	s_cselect_b64 s[6:7], -1, 0
	s_cmp_lg_u32 s4, 1
	v_lshl_add_u64 v[4:5], s[76:77], 0, v[132:133]
	s_cbranch_scc1 .LBB0_373
	s_barrier

;     __device__ __forceinline__ size_t aoff(const Unit& u) const { return (size_t)u.pm * a_tstep + (size_t)u.pn * a_pnstep; }
;     __device__ __forceinline__ size_t boff(const Unit& u) const { return (size_t)u.pn * b_tstep; }
;     __device__ __forceinline__ size_t boff(const Unit& u) const { return (size_t)u.pn * b_tstep; }
; #define PG8_GLOAD(dst0, dst1, lu) do { if constexpr (GATHER) { _Pragma("unroll") for (int _i = 0; _i < 2; ++_i) { dst0[_i] = S.toks[(lu) * 256 + rowA[_i]] + colA[_i]; dst1[_i] = S.toks[(lu) * 256 + 128 + rowA[_i]] + colA[_i]; } } } while (0)
; #define PG8_BIAS(u_, ui_) do { if constexpr (Epi::LDSBIAS) { if (wid == 0) __builtin_amdgcn_global_load_lds((const unsigned*)(E.bias_ptr(u_) + 4 * lane), (LAS unsigned*)(lds + BIAS_OFF + ((ui_) & 1) * 1024), 16, 0, 0); } } while (0)
; template <class Epi, class Sched, bool ALIGN_EPI, bool SP2, bool FP8 = false>
; __device__ __forceinline__ void gemm_phase(LAS unsigned char* lds, const Gemm g, const Sched& S, const Epi& E) {
;     ...
;         const bool has_next = S.next(ui + 1, nxt);
;         const char* nA = has_next ? (const char*)g.A + S.aoff(nxt) : cA; const char* nB = has_next ? (const char*)g.Bt + S.boff(nxt) : cB;
;         if constexpr (GATHER) { if (has_next) PG8_GLOAD(nG0, nG1, ui + 1); else { nG0[0] = cG0[0]; nG0[1] = cG0[1]; nG1[0] = cG1[0]; nG1[1] = cG1[1]; } }
; #pragma unroll 1
;         for (int t = 0; t < nt; t += 2) {
;             const bool last = (t == nt - 2);
;             const char* a1 = cA + (size_t)(t + 1) * kstep;
;             const char* a2 = last ? nA : cA + (size_t)(t + 2) * kstep; const char* b2 = last ? nB : cB + (size_t)(t + 2) * kstep;
;     ...
; #pragma unroll
;         for (int a = 0; a < 2; ++a)
; #pragma unroll
;             for (int b = 0; b < 2; ++b)
; #pragma unroll
;                 for (int m = 0; m < 4; ++m)
; #pragma unroll
;                     for (int n = 0; n < 2; ++n) acc[a][b][m][n] = (f32x4){0.f, 0.f, 0.f, 0.f};
;         cur = nxt; cA = nA; cB = nB; ++ui; PG8_BIAS(cur, ui);
.LBB0_378:
	s_nop 0
	v_cndmask_b32_e64 v2, 0, 1, s[4:5]
	v_cmp_ne_u32_e64 s[2:3], 1, v2
	s_andn2_b64 vcc, exec, s[4:5]
	s_mov_b64 s[4:5], s[76:77]
	s_cbranch_vccnz .LBB0_380
	s_mul_i32 s4, s75, 0x30000
	s_mul_hi_i32 s5, s75, 0x30000
	s_add_u32 s4, s73, s4
	s_addc_u32 s5, s79, s5
	s_cmp_gt_i32 s72, 7
	s_cselect_b32 s99, 0x100, 0
	s_add_u32 s4, s4, s99
	s_addc_u32 s5, s5, 0
.LBB0_380:
	s_and_b64 vcc, exec, s[2:3]
	s_mov_b64 s[16:17], s[80:81]
	s_cbranch_vccnz .LBB0_382
	s_mul_i32 s16, s72, 0x30000
	s_mul_hi_i32 s17, s72, 0x30000
	s_add_u32 s16, s39, s16
	s_addc_u32 s17, s40, s17
	s_cmp_gt_i32 s72, 7
	s_cselect_b32 s99, 0x100, 0
	s_add_u32 s16, s16, s99
	s_addc_u32 s17, s17, 0
.LBB0_382:
	s_add_u32 s83, s80, 0x100
	v_mov_b32_e32 v2, 0
	s_addc_u32 s84, s81, 0
	s_mov_b32 s85, s98
	s_cmp_gt_i32 s72, 7
	s_cselect_b32 s98, 0, 2
	v_mov_b32_e32 v3, v2
	v_mov_b32_e32 v4, v2
	v_mov_b32_e32 v5, v2
	v_mov_b32_e32 v6, v2
	v_mov_b32_e32 v7, v2
	v_mov_b32_e32 v8, v2
	v_mov_b32_e32 v9, v2
	v_mov_b32_e32 v10, v2
	v_mov_b32_e32 v11, v2
	v_mov_b32_e32 v12, v2
	v_mov_b32_e32 v13, v2
	v_mov_b32_e32 v18, v2
	v_mov_b32_e32 v19, v2
	v_mov_b32_e32 v20, v2
	v_mov_b32_e32 v21, v2
	v_mov_b32_e32 v26, v2
	v_mov_b32_e32 v27, v2
	v_mov_b32_e32 v28, v2
	v_mov_b32_e32 v29, v2
	v_mov_b32_e32 v34, v2
	v_mov_b32_e32 v35, v2
	v_mov_b32_e32 v36, v2
	v_mov_b32_e32 v37, v2
	v_mov_b32_e32 v42, v2
	v_mov_b32_e32 v43, v2
	v_mov_b32_e32 v44, v2
	v_mov_b32_e32 v45, v2
	v_mov_b32_e32 v50, v2
	v_mov_b32_e32 v51, v2
	v_mov_b32_e32 v52, v2
	v_mov_b32_e32 v53, v2
	v_mov_b32_e32 v14, v2
	v_mov_b32_e32 v15, v2
	v_mov_b32_e32 v16, v2
	v_mov_b32_e32 v17, v2
	v_mov_b32_e32 v22, v2
	v_mov_b32_e32 v23, v2
	v_mov_b32_e32 v24, v2
	v_mov_b32_e32 v25, v2
	v_mov_b32_e32 v30, v2
	v_mov_b32_e32 v31, v2
	v_mov_b32_e32 v32, v2
	v_mov_b32_e32 v33, v2
	v_mov_b32_e32 v38, v2
	v_mov_b32_e32 v39, v2
	v_mov_b32_e32 v40, v2
	v_mov_b32_e32 v41, v2
	v_mov_b32_e32 v46, v2
	v_mov_b32_e32 v47, v2
	v_mov_b32_e32 v48, v2
	v_mov_b32_e32 v49, v2
	v_mov_b32_e32 v54, v2
	v_mov_b32_e32 v55, v2
	v_mov_b32_e32 v56, v2
	v_mov_b32_e32 v57, v2
	v_mov_b32_e32 v58, v2
	v_mov_b32_e32 v59, v2
	v_mov_b32_e32 v60, v2
	v_mov_b32_e32 v61, v2
	v_mov_b32_e32 v62, v2
	v_mov_b32_e32 v63, v2
	v_mov_b32_e32 v64, v2
	v_mov_b32_e32 v65, v2
	v_mov_b32_e32 v66, v2
	v_mov_b32_e32 v67, v2
	v_mov_b32_e32 v68, v2
	v_mov_b32_e32 v69, v2
	v_mov_b32_e32 v70, v2
	v_mov_b32_e32 v71, v2
	v_mov_b32_e32 v72, v2
	v_mov_b32_e32 v73, v2
	v_mov_b32_e32 v74, v2
	v_mov_b32_e32 v75, v2
	v_mov_b32_e32 v76, v2
	v_mov_b32_e32 v77, v2
	v_mov_b32_e32 v82, v2
	v_mov_b32_e32 v83, v2
	v_mov_b32_e32 v84, v2
	v_mov_b32_e32 v85, v2
	v_mov_b32_e32 v90, v2
	v_mov_b32_e32 v91, v2
	v_mov_b32_e32 v92, v2
	v_mov_b32_e32 v93, v2
	v_mov_b32_e32 v98, v2
	v_mov_b32_e32 v99, v2
	v_mov_b32_e32 v100, v2
	v_mov_b32_e32 v101, v2
	v_mov_b32_e32 v106, v2
	v_mov_b32_e32 v107, v2
	v_mov_b32_e32 v108, v2
	v_mov_b32_e32 v109, v2
	v_mov_b32_e32 v114, v2
	v_mov_b32_e32 v115, v2
	v_mov_b32_e32 v116, v2
	v_mov_b32_e32 v117, v2
	v_mov_b32_e32 v78, v2
	v_mov_b32_e32 v79, v2
	v_mov_b32_e32 v80, v2
	v_mov_b32_e32 v81, v2
	v_mov_b32_e32 v86, v2
	v_mov_b32_e32 v87, v2
	v_mov_b32_e32 v88, v2
	v_mov_b32_e32 v89, v2
	v_mov_b32_e32 v94, v2
	v_mov_b32_e32 v95, v2
	v_mov_b32_e32 v96, v2
	v_mov_b32_e32 v97, v2
	v_mov_b32_e32 v102, v2
	v_mov_b32_e32 v103, v2
	v_mov_b32_e32 v104, v2
	v_mov_b32_e32 v105, v2
	v_mov_b32_e32 v110, v2
	v_mov_b32_e32 v111, v2
	v_mov_b32_e32 v112, v2
	v_mov_b32_e32 v113, v2
	v_mov_b32_e32 v118, v2
	v_mov_b32_e32 v119, v2
	v_mov_b32_e32 v120, v2
	v_mov_b32_e32 v121, v2
	v_mov_b32_e32 v122, v2
	v_mov_b32_e32 v123, v2
	v_mov_b32_e32 v124, v2
	v_mov_b32_e32 v125, v2
	v_mov_b32_e32 v126, v2
	v_mov_b32_e32 v127, v2
	v_mov_b32_e32 v128, v2
	v_mov_b32_e32 v129, v2
